# down-projection epilogues (both MoE layers) rewritten: row gates fetched one unit ahead, lane-pair exchange gives 16-byte stores
# speedup vs baseline: 1.0135x; 1.0135x over previous
; #define PG8_STAGE(bufoff, gbase, voff) do { const char* gb_ = PG8_UNI(gbase);     \
;         _Pragma("unroll") for (int _i = 0; _i < 2; ++_i) \
;         __builtin_amdgcn_global_load_lds((const unsigned*)(gb_ + (voff)[_i]), (PG8_LAS unsigned*)(lds + (bufoff) + ldsw + _i * 8192), 16, 0, 0); } while (0)
; #define PG8_STAGE_A(bufoff, kptr, h) do { if constexpr (GATHER) { PG8_STAGE(bufoff, kptr, vA[h]); } else { PG8_STAGE(bufoff, (kptr) + (h) * hstep, voffA); } } while (0)
; #define PG8_WAIT_V(n) asm volatile("s_waitcnt vmcnt(" #n ")" ::: "memory")
; #define PG8_BAR __builtin_amdgcn_s_barrier()
; template <class Epi, class Sched, bool ALIGN_EPI = false, bool SP2 = false, bool GATHER = false, bool F8 = false>
; __device__ __forceinline__ void gemm_phase(PG8_LAS unsigned char* lds, const Gemm g, const Sched& S, const Epi& E) {
;     ...
;     if constexpr (SP2) {
;         PG8_STAGE(PG8_SB(0, 0), cB, voffB); PG8_STAGE(PG8_SB(0, 1), cB + hstep, voffB); PG8_STAGE_A(PG8_SA(0, 0), cA, 0); PG8_STAGE_A(PG8_SA(0, 1), cA, 1);
;         if (wr == 1) PG8_BAR;
;         PG8_WAIT_V(2); PG8_BAR;
;         PG8_STAGE(PG8_SB(1, 0), cB + kstep, voffB); PG8_STAGE_A(PG8_SA(1, 0), cA + kstep, 0); PG8_STAGE(PG8_SB(1, 1), cB + hstep + kstep, voffB);
;         PG8_WAIT_V(6); PG8_BAR;
;     DI void operator()(const f32x4 (&acc)[2][2][4][2], const Unit& u, int wr, int wc, int fr, int fq) const {
;         const int row0 = u.pm * 256 + wr * 64 + fr, col0 = (u.pn & 7) * 256 + wc * 32 + 8 * fq;
;         float gts[2][4];
; #pragma unroll
;         for (int ai = 0; ai < 2; ++ai)
; #pragma unroll
;             for (int m = 0; m < 4; ++m) gts[ai][m] = gatev[row0 + ai * 128 + m * 16];
.LBB0_946:
	s_add_u32 s12, s18, 0x80
	s_addc_u32 s13, s19, 0
	s_add_u32 s14, s94, 0x80
	s_addc_u32 s15, s95, 0
	s_add_u32 s20, s18, 0x20080
	s_addc_u32 s21, s19, 0
	s_add_i32 m0, s28, 0x18000
	v_lshl_add_u64 v[6:7], s[12:13], 0, v[200:201]
	s_waitcnt vmcnt(2)
	s_barrier
	global_load_lds_dwordx4 v[6:7], off
	v_lshl_add_u64 v[6:7], s[12:13], 0, v[198:199]
	s_add_i32 m0, s28, 0x1a000
	s_add_i32 s39, s28, 0x8000
	global_load_lds_dwordx4 v[6:7], off
	v_lshl_add_u64 v[6:7], s[14:15], 0, v[204:205]
	s_mov_b32 m0, s39
	s_add_i32 s56, s28, 0xa000
	global_load_lds_dwordx4 v[6:7], off
	v_lshl_add_u64 v[6:7], s[14:15], 0, v[206:207]
	s_mov_b32 m0, s56
	v_and_b32_e32 v5, 15, v0
	global_load_lds_dwordx4 v[6:7], off
	s_add_i32 m0, s28, 0x1c000
	v_lshl_add_u64 v[6:7], s[20:21], 0, v[200:201]
	global_load_lds_dwordx4 v[6:7], off
	v_lshl_add_u64 v[6:7], s[20:21], 0, v[198:199]
	s_add_i32 m0, s28, 0x1e000
	v_and_b32_e32 v8, 32, v195
	global_load_lds_dwordx4 v[6:7], off
	v_lshlrev_b32_e32 v6, 1, v4
	v_lshl_or_b32 v205, s10, 6, v5
	v_lshl_or_b32 v5, v5, 6, v6
	s_lshl_b32 s10, s10, 13
	s_lshl_b32 s9, s9, 5
	v_lshlrev_b32_e32 v7, 6, v0
	s_movk_i32 s11, 0x3c0
	v_bitop3_b32 v5, v5, s10, v8 bitop3:0xde
	s_and_b32 s10, s9, 0x60
	v_and_or_b32 v7, v7, s11, v6
	s_lshl_b32 s9, s10, 7
	v_bitop3_b32 v207, s9, v7, v8 bitop3:0xf6
	s_waitcnt vmcnt(6)
	s_cmpk_lt_u32 s8, 0x100
	v_lshlrev_b32_e32 v212, 2, v2
	v_add_u32_e32 v2, 0, v207
	s_cselect_b64 s[8:9], -1, 0
	v_or_b32_e32 v214, s10, v4
	v_lshlrev_b32_e32 v210, 2, v3
	v_add_u32_e32 v215, 0x10000, v2
	v_add_u32_e32 v216, 0x14000, v2
	v_add_u32_e32 v217, 0, v5
	v_mov_b32_e32 v218, 0x7f7f7f7f
	s_mov_b32 s57, 0xc3e00000
	v_mov_b32_e32 v219, 0x43e00000
	s_barrier
	v_lshl_add_u32 v225, s59, 8, v205
	v_lshlrev_b32_e32 v225, 2, v225
	global_load_dword v240, v225, s[60:61]
	global_load_dword v241, v225, s[60:61] offset:64
	global_load_dword v242, v225, s[60:61] offset:128
	global_load_dword v243, v225, s[60:61] offset:192
	global_load_dword v244, v225, s[60:61] offset:512
	global_load_dword v245, v225, s[60:61] offset:576
	global_load_dword v246, v225, s[60:61] offset:640
	global_load_dword v247, v225, s[60:61] offset:704
	s_branch .LBB0_949

;     DI void operator()(const f32x4 (&acc)[2][2][4][2], const Unit& u, int wr, int wc, int fr, int fq) const {
;         const int row0 = u.pm * 256 + wr * 64 + fr, col0 = (u.pn & 7) * 256 + wc * 32 + 8 * fq;
;         float gts[2][4];
; #pragma unroll
;         for (int ai = 0; ai < 2; ++ai)
; #pragma unroll
;             for (int m = 0; m < 4; ++m) gts[ai][m] = gatev[row0 + ai * 128 + m * 16];
;         __builtin_amdgcn_sched_barrier(0);
; #pragma unroll
;         for (int ai = 0; ai < 2; ++ai)
; #pragma unroll
;             for (int m = 0; m < 4; ++m) { const int row = row0 + ai * 128 + m * 16; const float gt = gts[ai][m] * ws;
; #pragma unroll
;                 for (int bj = 0; bj < 2; ++bj) { const f32x4 v0 = acc[ai][bj][m][0] * gt, v1 = acc[ai][bj][m][1] * gt;
;                     u32x2 w; w.x = pk4_fp8(v0[0], v0[1], v0[2], v0[3]); w.y = pk4_fp8(v1[0], v1[1], v1[2], v1[3]);
;                     *(u32x2*)((unsigned char*)Y + (size_t)row * DM + col0 + bj * 128) = w; } }
.LBB0_959:
	s_andn2_b64 vcc, exec, s[12:13]
	s_cbranch_vccnz .Lp9_nopf
	v_lshl_add_u32 v225, s58, 8, v205
	v_lshlrev_b32_e32 v225, 2, v225
	global_load_dword v232, v225, s[60:61]
	global_load_dword v233, v225, s[60:61] offset:64
	global_load_dword v234, v225, s[60:61] offset:128
	global_load_dword v235, v225, s[60:61] offset:192
	global_load_dword v236, v225, s[60:61] offset:512
	global_load_dword v237, v225, s[60:61] offset:576
	global_load_dword v238, v225, s[60:61] offset:640
	global_load_dword v239, v225, s[60:61] offset:704
.Lp9_nopf:
	v_and_b32_e32 v30, 8, v214
	v_lshlrev_b32_e32 v30, 1, v30
	v_add_u32_e32 v30, v30, v205
	v_lshl_add_u32 v30, s59, 8, v30
	v_lshlrev_b32_e32 v224, 11, v30
	s_lshl_b32 s11, s16, 8
	s_and_b32 s11, s11, 0x700
	v_and_b32_e32 v30, 0x70, v214
	v_or_b32_e32 v30, s11, v30
	v_add_u32_e32 v224, v224, v30
	v_add_f32_e32 v26, v240, v240
	v_add_f32_e32 v28, v241, v241
	v_pk_mul_f32 v[2:3], v[190:191], v[26:27] op_sel_hi:[1,0]
	v_pk_mul_f32 v[4:5], v[192:193], v[26:27] op_sel_hi:[1,0]
	v_pk_mul_f32 v[6:7], v[186:187], v[26:27] op_sel_hi:[1,0]
	v_pk_mul_f32 v[8:9], v[188:189], v[26:27] op_sel_hi:[1,0]
	v_pk_mul_f32 v[10:11], v[174:175], v[28:29] op_sel_hi:[1,0]
	v_pk_mul_f32 v[12:13], v[176:177], v[28:29] op_sel_hi:[1,0]
	v_pk_mul_f32 v[14:15], v[170:171], v[28:29] op_sel_hi:[1,0]
	v_pk_mul_f32 v[16:17], v[172:173], v[28:29] op_sel_hi:[1,0]
	v_med3_f32 v2, v2, s57, v219
	v_med3_f32 v3, v3, s57, v219
	v_med3_f32 v4, v4, s57, v219
	v_med3_f32 v5, v5, s57, v219
	v_med3_f32 v6, v6, s57, v219
	v_med3_f32 v7, v7, s57, v219
	v_med3_f32 v8, v8, s57, v219
	v_med3_f32 v9, v9, s57, v219
	v_med3_f32 v10, v10, s57, v219
	v_med3_f32 v11, v11, s57, v219
	v_med3_f32 v12, v12, s57, v219
	v_med3_f32 v13, v13, s57, v219
	v_med3_f32 v14, v14, s57, v219
	v_med3_f32 v15, v15, s57, v219
	v_med3_f32 v16, v16, s57, v219
	v_med3_f32 v17, v17, s57, v219
	v_cvt_pk_fp8_f32 v18, v2, v3
	v_cvt_pk_fp8_f32 v19, v6, v7
	v_cvt_pk_fp8_f32 v20, v10, v11
	v_cvt_pk_fp8_f32 v21, v14, v15
	v_cvt_pk_fp8_f32 v18, v4, v5 op_sel:[0,0,1]
	v_cvt_pk_fp8_f32 v19, v8, v9 op_sel:[0,0,1]
	v_cvt_pk_fp8_f32 v20, v12, v13 op_sel:[0,0,1]
	v_cvt_pk_fp8_f32 v21, v16, v17 op_sel:[0,0,1]
	v_pk_mul_f32 v[2:3], v[182:183], v[26:27] op_sel_hi:[1,0]
	v_pk_mul_f32 v[4:5], v[184:185], v[26:27] op_sel_hi:[1,0]
	v_pk_mul_f32 v[6:7], v[178:179], v[26:27] op_sel_hi:[1,0]
	v_pk_mul_f32 v[8:9], v[180:181], v[26:27] op_sel_hi:[1,0]
	v_pk_mul_f32 v[10:11], v[166:167], v[28:29] op_sel_hi:[1,0]
	v_pk_mul_f32 v[12:13], v[168:169], v[28:29] op_sel_hi:[1,0]
	v_pk_mul_f32 v[14:15], v[162:163], v[28:29] op_sel_hi:[1,0]
	v_pk_mul_f32 v[16:17], v[164:165], v[28:29] op_sel_hi:[1,0]
	v_med3_f32 v2, v2, s57, v219
	v_med3_f32 v3, v3, s57, v219
	v_med3_f32 v4, v4, s57, v219
	v_med3_f32 v5, v5, s57, v219
	v_med3_f32 v6, v6, s57, v219
	v_med3_f32 v7, v7, s57, v219
	v_med3_f32 v8, v8, s57, v219
	v_med3_f32 v9, v9, s57, v219
	v_med3_f32 v10, v10, s57, v219
	v_med3_f32 v11, v11, s57, v219
	v_med3_f32 v12, v12, s57, v219
	v_med3_f32 v13, v13, s57, v219
	v_med3_f32 v14, v14, s57, v219
	v_med3_f32 v15, v15, s57, v219
	v_med3_f32 v16, v16, s57, v219
	v_med3_f32 v17, v17, s57, v219
	v_cvt_pk_fp8_f32 v22, v2, v3
	v_cvt_pk_fp8_f32 v23, v6, v7
	v_cvt_pk_fp8_f32 v24, v10, v11
	v_cvt_pk_fp8_f32 v25, v14, v15
	v_cvt_pk_fp8_f32 v22, v4, v5 op_sel:[0,0,1]
	v_cvt_pk_fp8_f32 v23, v8, v9 op_sel:[0,0,1]
	v_cvt_pk_fp8_f32 v24, v12, v13 op_sel:[0,0,1]
	v_cvt_pk_fp8_f32 v25, v16, v17 op_sel:[0,0,1]
	s_nop 1
	v_permlane16_swap_b32_e32 v18, v20
	v_permlane16_swap_b32_e32 v19, v21
	v_mov_b32_e32 v30, v224
	global_store_dwordx4 v30, v[18:21], s[4:5]
	s_nop 1
	v_permlane16_swap_b32_e32 v22, v24
	v_permlane16_swap_b32_e32 v23, v25
	v_add_u32_e32 v30, 0x80, v224
	global_store_dwordx4 v30, v[22:25], s[4:5]
	v_add_f32_e32 v26, v242, v242
	v_add_f32_e32 v28, v243, v243
	v_pk_mul_f32 v[2:3], v[158:159], v[26:27] op_sel_hi:[1,0]
	v_pk_mul_f32 v[4:5], v[160:161], v[26:27] op_sel_hi:[1,0]
	v_pk_mul_f32 v[6:7], v[154:155], v[26:27] op_sel_hi:[1,0]
	v_pk_mul_f32 v[8:9], v[156:157], v[26:27] op_sel_hi:[1,0]
	v_pk_mul_f32 v[10:11], v[142:143], v[28:29] op_sel_hi:[1,0]
	v_pk_mul_f32 v[12:13], v[144:145], v[28:29] op_sel_hi:[1,0]
	v_pk_mul_f32 v[14:15], v[138:139], v[28:29] op_sel_hi:[1,0]
	v_pk_mul_f32 v[16:17], v[140:141], v[28:29] op_sel_hi:[1,0]
	v_med3_f32 v2, v2, s57, v219
	v_med3_f32 v3, v3, s57, v219
	v_med3_f32 v4, v4, s57, v219
	v_med3_f32 v5, v5, s57, v219
	v_med3_f32 v6, v6, s57, v219
	v_med3_f32 v7, v7, s57, v219
	v_med3_f32 v8, v8, s57, v219
	v_med3_f32 v9, v9, s57, v219
	v_med3_f32 v10, v10, s57, v219
	v_med3_f32 v11, v11, s57, v219
	v_med3_f32 v12, v12, s57, v219
	v_med3_f32 v13, v13, s57, v219
	v_med3_f32 v14, v14, s57, v219
	v_med3_f32 v15, v15, s57, v219
	v_med3_f32 v16, v16, s57, v219
	v_med3_f32 v17, v17, s57, v219
	v_cvt_pk_fp8_f32 v18, v2, v3
	v_cvt_pk_fp8_f32 v19, v6, v7
	v_cvt_pk_fp8_f32 v20, v10, v11
	v_cvt_pk_fp8_f32 v21, v14, v15
	v_cvt_pk_fp8_f32 v18, v4, v5 op_sel:[0,0,1]
	v_cvt_pk_fp8_f32 v19, v8, v9 op_sel:[0,0,1]
	v_cvt_pk_fp8_f32 v20, v12, v13 op_sel:[0,0,1]
	v_cvt_pk_fp8_f32 v21, v16, v17 op_sel:[0,0,1]
	v_pk_mul_f32 v[2:3], v[150:151], v[26:27] op_sel_hi:[1,0]
	v_pk_mul_f32 v[4:5], v[152:153], v[26:27] op_sel_hi:[1,0]
	v_pk_mul_f32 v[6:7], v[146:147], v[26:27] op_sel_hi:[1,0]
	v_pk_mul_f32 v[8:9], v[148:149], v[26:27] op_sel_hi:[1,0]
	v_pk_mul_f32 v[10:11], v[134:135], v[28:29] op_sel_hi:[1,0]
	v_pk_mul_f32 v[12:13], v[136:137], v[28:29] op_sel_hi:[1,0]
	v_pk_mul_f32 v[14:15], v[130:131], v[28:29] op_sel_hi:[1,0]
	v_pk_mul_f32 v[16:17], v[132:133], v[28:29] op_sel_hi:[1,0]
	v_med3_f32 v2, v2, s57, v219
;     DI void operator()(const f32x4 (&acc)[2][2][4][2], const Unit& u, int wr, int wc, int fr, int fq) const {
;     ...
;             for (int m = 0; m < 4; ++m) { const int row = row0 + ai * 128 + m * 16; const float gt = gts[ai][m] * ws;
; #pragma unroll
;                 for (int bj = 0; bj < 2; ++bj) { const f32x4 v0 = acc[ai][bj][m][0] * gt, v1 = acc[ai][bj][m][1] * gt;
;                     u32x2 w; w.x = pk4_fp8(v0[0], v0[1], v0[2], v0[3]); w.y = pk4_fp8(v1[0], v1[1], v1[2], v1[3]);
;                     *(u32x2*)((unsigned char*)Y + (size_t)row * DM + col0 + bj * 128) = w; } }
	v_med3_f32 v3, v3, s57, v219
	v_med3_f32 v4, v4, s57, v219
	v_med3_f32 v5, v5, s57, v219
	v_med3_f32 v6, v6, s57, v219
	v_med3_f32 v7, v7, s57, v219
	v_med3_f32 v8, v8, s57, v219
	v_med3_f32 v9, v9, s57, v219
	v_med3_f32 v10, v10, s57, v219
	v_med3_f32 v11, v11, s57, v219
	v_med3_f32 v12, v12, s57, v219
	v_med3_f32 v13, v13, s57, v219
	v_med3_f32 v14, v14, s57, v219
	v_med3_f32 v15, v15, s57, v219
	v_med3_f32 v16, v16, s57, v219
	v_med3_f32 v17, v17, s57, v219
	v_cvt_pk_fp8_f32 v22, v2, v3
	v_cvt_pk_fp8_f32 v23, v6, v7
	v_cvt_pk_fp8_f32 v24, v10, v11
	v_cvt_pk_fp8_f32 v25, v14, v15
	v_cvt_pk_fp8_f32 v22, v4, v5 op_sel:[0,0,1]
	v_cvt_pk_fp8_f32 v23, v8, v9 op_sel:[0,0,1]
	v_cvt_pk_fp8_f32 v24, v12, v13 op_sel:[0,0,1]
	v_cvt_pk_fp8_f32 v25, v16, v17 op_sel:[0,0,1]
	s_nop 1
	v_permlane16_swap_b32_e32 v18, v20
	v_permlane16_swap_b32_e32 v19, v21
	v_add_u32_e32 v30, 0x10000, v224
	global_store_dwordx4 v30, v[18:21], s[4:5]
	s_nop 1
	v_permlane16_swap_b32_e32 v22, v24
	v_permlane16_swap_b32_e32 v23, v25
	v_add_u32_e32 v30, 0x10080, v224
	global_store_dwordx4 v30, v[22:25], s[4:5]
	v_add_f32_e32 v26, v244, v244
	v_add_f32_e32 v28, v245, v245
	v_pk_mul_f32 v[2:3], v[126:127], v[26:27] op_sel_hi:[1,0]
	v_pk_mul_f32 v[4:5], v[128:129], v[26:27] op_sel_hi:[1,0]
	v_pk_mul_f32 v[6:7], v[122:123], v[26:27] op_sel_hi:[1,0]
	v_pk_mul_f32 v[8:9], v[124:125], v[26:27] op_sel_hi:[1,0]
	v_pk_mul_f32 v[10:11], v[110:111], v[28:29] op_sel_hi:[1,0]
	v_pk_mul_f32 v[12:13], v[112:113], v[28:29] op_sel_hi:[1,0]
	v_pk_mul_f32 v[14:15], v[106:107], v[28:29] op_sel_hi:[1,0]
	v_pk_mul_f32 v[16:17], v[108:109], v[28:29] op_sel_hi:[1,0]
	v_med3_f32 v2, v2, s57, v219
	v_med3_f32 v3, v3, s57, v219
	v_med3_f32 v4, v4, s57, v219
	v_med3_f32 v5, v5, s57, v219
	v_med3_f32 v6, v6, s57, v219
	v_med3_f32 v7, v7, s57, v219
	v_med3_f32 v8, v8, s57, v219
	v_med3_f32 v9, v9, s57, v219
	v_med3_f32 v10, v10, s57, v219
	v_med3_f32 v11, v11, s57, v219
	v_med3_f32 v12, v12, s57, v219
	v_med3_f32 v13, v13, s57, v219
	v_med3_f32 v14, v14, s57, v219
	v_med3_f32 v15, v15, s57, v219
	v_med3_f32 v16, v16, s57, v219
	v_med3_f32 v17, v17, s57, v219
	v_cvt_pk_fp8_f32 v18, v2, v3
	v_cvt_pk_fp8_f32 v19, v6, v7
	v_cvt_pk_fp8_f32 v20, v10, v11
	v_cvt_pk_fp8_f32 v21, v14, v15
	v_cvt_pk_fp8_f32 v18, v4, v5 op_sel:[0,0,1]
	v_cvt_pk_fp8_f32 v19, v8, v9 op_sel:[0,0,1]
	v_cvt_pk_fp8_f32 v20, v12, v13 op_sel:[0,0,1]
	v_cvt_pk_fp8_f32 v21, v16, v17 op_sel:[0,0,1]
	v_pk_mul_f32 v[2:3], v[118:119], v[26:27] op_sel_hi:[1,0]
	v_pk_mul_f32 v[4:5], v[120:121], v[26:27] op_sel_hi:[1,0]
	v_pk_mul_f32 v[6:7], v[114:115], v[26:27] op_sel_hi:[1,0]
	v_pk_mul_f32 v[8:9], v[116:117], v[26:27] op_sel_hi:[1,0]
	v_pk_mul_f32 v[10:11], v[94:95], v[28:29] op_sel_hi:[1,0]
	v_pk_mul_f32 v[12:13], v[96:97], v[28:29] op_sel_hi:[1,0]
	v_pk_mul_f32 v[14:15], v[82:83], v[28:29] op_sel_hi:[1,0]
	v_pk_mul_f32 v[16:17], v[84:85], v[28:29] op_sel_hi:[1,0]
	v_med3_f32 v2, v2, s57, v219
	v_med3_f32 v3, v3, s57, v219
	v_med3_f32 v4, v4, s57, v219
	v_med3_f32 v5, v5, s57, v219
	v_med3_f32 v6, v6, s57, v219
	v_med3_f32 v7, v7, s57, v219
	v_med3_f32 v8, v8, s57, v219
	v_med3_f32 v9, v9, s57, v219
	v_med3_f32 v10, v10, s57, v219
	v_med3_f32 v11, v11, s57, v219
	v_med3_f32 v12, v12, s57, v219
	v_med3_f32 v13, v13, s57, v219
	v_med3_f32 v14, v14, s57, v219
	v_med3_f32 v15, v15, s57, v219
	v_med3_f32 v16, v16, s57, v219
	v_med3_f32 v17, v17, s57, v219
	v_cvt_pk_fp8_f32 v22, v2, v3
	v_cvt_pk_fp8_f32 v23, v6, v7
	v_cvt_pk_fp8_f32 v24, v10, v11
	v_cvt_pk_fp8_f32 v25, v14, v15
	v_cvt_pk_fp8_f32 v22, v4, v5 op_sel:[0,0,1]
	v_cvt_pk_fp8_f32 v23, v8, v9 op_sel:[0,0,1]
	v_cvt_pk_fp8_f32 v24, v12, v13 op_sel:[0,0,1]
	v_cvt_pk_fp8_f32 v25, v16, v17 op_sel:[0,0,1]
	s_nop 1
	v_permlane16_swap_b32_e32 v18, v20
	v_permlane16_swap_b32_e32 v19, v21
	v_add_u32_e32 v30, 0x40000, v224
	global_store_dwordx4 v30, v[18:21], s[4:5]
	s_nop 1
	v_permlane16_swap_b32_e32 v22, v24
	v_permlane16_swap_b32_e32 v23, v25
	v_add_u32_e32 v30, 0x40080, v224
	global_store_dwordx4 v30, v[22:25], s[4:5]
	v_add_f32_e32 v26, v246, v246
	v_add_f32_e32 v28, v247, v247
	v_pk_mul_f32 v[2:3], v[90:91], v[26:27] op_sel_hi:[1,0]
	v_pk_mul_f32 v[4:5], v[92:93], v[26:27] op_sel_hi:[1,0]
	v_pk_mul_f32 v[6:7], v[86:87], v[26:27] op_sel_hi:[1,0]
	v_pk_mul_f32 v[8:9], v[88:89], v[26:27] op_sel_hi:[1,0]
	v_pk_mul_f32 v[10:11], v[70:71], v[28:29] op_sel_hi:[1,0]
	v_pk_mul_f32 v[12:13], v[72:73], v[28:29] op_sel_hi:[1,0]
	v_pk_mul_f32 v[14:15], v[66:67], v[28:29] op_sel_hi:[1,0]
	v_pk_mul_f32 v[16:17], v[68:69], v[28:29] op_sel_hi:[1,0]
	v_med3_f32 v2, v2, s57, v219
	v_med3_f32 v3, v3, s57, v219
	v_med3_f32 v4, v4, s57, v219
	v_med3_f32 v5, v5, s57, v219
	v_med3_f32 v6, v6, s57, v219
	v_med3_f32 v7, v7, s57, v219
	v_med3_f32 v8, v8, s57, v219
	v_med3_f32 v9, v9, s57, v219
	v_med3_f32 v10, v10, s57, v219
	v_med3_f32 v11, v11, s57, v219
	v_med3_f32 v12, v12, s57, v219
	v_med3_f32 v13, v13, s57, v219
	v_med3_f32 v14, v14, s57, v219
	v_med3_f32 v15, v15, s57, v219
	v_med3_f32 v16, v16, s57, v219
	v_med3_f32 v17, v17, s57, v219
	v_cvt_pk_fp8_f32 v18, v2, v3
	v_cvt_pk_fp8_f32 v19, v6, v7
	v_cvt_pk_fp8_f32 v20, v10, v11
	v_cvt_pk_fp8_f32 v21, v14, v15
	v_cvt_pk_fp8_f32 v18, v4, v5 op_sel:[0,0,1]
	v_cvt_pk_fp8_f32 v19, v8, v9 op_sel:[0,0,1]
	v_cvt_pk_fp8_f32 v20, v12, v13 op_sel:[0,0,1]
	v_cvt_pk_fp8_f32 v21, v16, v17 op_sel:[0,0,1]
	v_pk_mul_f32 v[2:3], v[98:99], v[26:27] op_sel_hi:[1,0]
	v_pk_mul_f32 v[4:5], v[100:101], v[26:27] op_sel_hi:[1,0]
	v_pk_mul_f32 v[6:7], v[102:103], v[26:27] op_sel_hi:[1,0]
	v_pk_mul_f32 v[8:9], v[104:105], v[26:27] op_sel_hi:[1,0]
	v_pk_mul_f32 v[10:11], v[74:75], v[28:29] op_sel_hi:[1,0]
	v_pk_mul_f32 v[12:13], v[76:77], v[28:29] op_sel_hi:[1,0]
	v_pk_mul_f32 v[14:15], v[78:79], v[28:29] op_sel_hi:[1,0]
	v_pk_mul_f32 v[16:17], v[80:81], v[28:29] op_sel_hi:[1,0]
	v_med3_f32 v2, v2, s57, v219
	v_med3_f32 v3, v3, s57, v219
	v_med3_f32 v4, v4, s57, v219
	v_med3_f32 v5, v5, s57, v219
	v_med3_f32 v6, v6, s57, v219
	v_med3_f32 v7, v7, s57, v219
	v_med3_f32 v8, v8, s57, v219
	v_med3_f32 v9, v9, s57, v219
	v_med3_f32 v10, v10, s57, v219
	v_med3_f32 v11, v11, s57, v219
	v_med3_f32 v12, v12, s57, v219
	v_med3_f32 v13, v13, s57, v219
	v_med3_f32 v14, v14, s57, v219
	v_med3_f32 v15, v15, s57, v219
	v_med3_f32 v16, v16, s57, v219
	v_med3_f32 v17, v17, s57, v219
	v_cvt_pk_fp8_f32 v22, v2, v3
	v_cvt_pk_fp8_f32 v23, v6, v7
	v_cvt_pk_fp8_f32 v24, v10, v11
	v_cvt_pk_fp8_f32 v25, v14, v15
	v_cvt_pk_fp8_f32 v22, v4, v5 op_sel:[0,0,1]
	v_cvt_pk_fp8_f32 v23, v8, v9 op_sel:[0,0,1]
	v_cvt_pk_fp8_f32 v24, v12, v13 op_sel:[0,0,1]
	v_cvt_pk_fp8_f32 v25, v16, v17 op_sel:[0,0,1]
	s_nop 1
	v_permlane16_swap_b32_e32 v18, v20
	v_permlane16_swap_b32_e32 v19, v21
	v_add_u32_e32 v30, 0x50000, v224
	global_store_dwordx4 v30, v[18:21], s[4:5]
	s_nop 1
	v_permlane16_swap_b32_e32 v22, v24
	v_permlane16_swap_b32_e32 v23, v25
	v_add_u32_e32 v30, 0x50080, v224
	global_store_dwordx4 v30, v[22:25], s[4:5]
	s_andn2_b64 vcc, exec, s[12:13]
	s_cbranch_vccnz .Lp9_nocp
; #define PG8_BAR __builtin_amdgcn_s_barrier()
; template <class Epi, class Sched, bool ALIGN_EPI = false, bool SP2 = false, bool GATHER = false, bool F8 = false>
; __device__ __forceinline__ void gemm_phase(PG8_LAS unsigned char* lds, const Gemm g, const Sched& S, const Epi& E) {
;     ...
;         if constexpr (!Epi::AFTER_DRAIN) { E(acc, cur, wr, wc, fr, fq); S.done(cur); }
;         if (!has_next) break;
; #pragma unroll
;         for (int a = 0; a < 2; ++a)
; #pragma unroll
;             for (int b = 0; b < 2; ++b)
; #pragma unroll
;                 for (int m = 0; m < 4; ++m)
; #pragma unroll
;                     for (int n = 0; n < 2; ++n) acc[a][b][m][n] = (f32x4){0.f, 0.f, 0.f, 0.f};
;         cur = nxt; cA = nA; cB = nB; ++ui;
;         if constexpr (ALIGN_EPI) { if (wr == 1) PG8_BAR; }
	s_waitcnt vmcnt(8)
	v_mov_b32_e32 v240, v232
	v_mov_b32_e32 v241, v233
	v_mov_b32_e32 v242, v234
	v_mov_b32_e32 v243, v235
	v_mov_b32_e32 v244, v236
	v_mov_b32_e32 v245, v237
	v_mov_b32_e32 v246, v238
	v_mov_b32_e32 v247, v239
.Lp9_nocp:
	s_andn2_b64 vcc, exec, s[12:13]
	s_mov_b64 s[12:13], -1
	s_cbranch_vccnz .LBB0_948
	s_andn2_b64 vcc, exec, s[6:7]
	s_cbranch_vccnz .LBB0_947
	s_barrier
	s_branch .LBB0_947

; #define PG8_STAGE(bufoff, gbase, voff) do { const char* gb_ = PG8_UNI(gbase);     \
;         _Pragma("unroll") for (int _i = 0; _i < 2; ++_i) \
;         __builtin_amdgcn_global_load_lds((const unsigned*)(gb_ + (voff)[_i]), (PG8_LAS unsigned*)(lds + (bufoff) + ldsw + _i * 8192), 16, 0, 0); } while (0)
; #define PG8_STAGE_A(bufoff, kptr, h) do { if constexpr (GATHER) { PG8_STAGE(bufoff, kptr, vA[h]); } else { PG8_STAGE(bufoff, (kptr) + (h) * hstep, voffA); } } while (0)
; #define PG8_WAIT_V(n) asm volatile("s_waitcnt vmcnt(" #n ")" ::: "memory")
; #define PG8_BAR __builtin_amdgcn_s_barrier()
; template <class Epi, class Sched, bool ALIGN_EPI = false, bool SP2 = false, bool GATHER = false, bool F8 = false>
; __device__ __forceinline__ void gemm_phase(PG8_LAS unsigned char* lds, const Gemm g, const Sched& S, const Epi& E) {
;     ...
;     if constexpr (SP2) {
;         PG8_STAGE(PG8_SB(0, 0), cB, voffB); PG8_STAGE(PG8_SB(0, 1), cB + hstep, voffB); PG8_STAGE_A(PG8_SA(0, 0), cA, 0); PG8_STAGE_A(PG8_SA(0, 1), cA, 1);
;         if (wr == 1) PG8_BAR;
;         PG8_WAIT_V(2); PG8_BAR;
;         PG8_STAGE(PG8_SB(1, 0), cB + kstep, voffB); PG8_STAGE_A(PG8_SA(1, 0), cA + kstep, 0); PG8_STAGE(PG8_SB(1, 1), cB + hstep + kstep, voffB);
;         PG8_WAIT_V(6); PG8_BAR;
;     DI void operator()(const f32x4 (&acc)[2][2][4][2], const Unit& u, int wr, int wc, int fr, int fq) const {
;         const int row0 = u.pm * 256 + wr * 64 + fr, col0 = (u.pn & 7) * 256 + wc * 32 + 8 * fq;
;         float gts[2][4];
; #pragma unroll
;         for (int ai = 0; ai < 2; ++ai)
; #pragma unroll
;             for (int m = 0; m < 4; ++m) gts[ai][m] = gatev[row0 + ai * 128 + m * 16];
.LBB0_1955:
	s_add_u32 s12, s26, 0x80
	s_addc_u32 s13, s27, 0
	s_add_u32 s14, s94, 0x80
	s_addc_u32 s15, s95, 0
	s_add_u32 s16, s26, 0x20080
	s_addc_u32 s17, s27, 0
	s_add_i32 m0, s39, 0x18000
	v_lshl_add_u64 v[6:7], s[12:13], 0, v[198:199]
	s_waitcnt vmcnt(2)
	s_barrier
	global_load_lds_dwordx4 v[6:7], off
	v_lshl_add_u64 v[6:7], s[12:13], 0, v[196:197]
	s_add_i32 m0, s39, 0x1a000
	s_add_i32 s50, s39, 0x8000
	global_load_lds_dwordx4 v[6:7], off
	v_lshl_add_u64 v[6:7], s[14:15], 0, v[202:203]
	s_mov_b32 m0, s50
	s_add_i32 s51, s39, 0xa000
	global_load_lds_dwordx4 v[6:7], off
	v_lshl_add_u64 v[6:7], s[14:15], 0, v[204:205]
	s_mov_b32 m0, s51
	v_and_b32_e32 v5, 15, v0
	global_load_lds_dwordx4 v[6:7], off
	s_add_i32 m0, s39, 0x1c000
	v_lshl_add_u64 v[6:7], s[16:17], 0, v[198:199]
	global_load_lds_dwordx4 v[6:7], off
	v_lshl_add_u64 v[6:7], s[16:17], 0, v[196:197]
	s_add_i32 m0, s39, 0x1e000
	v_lshlrev_b32_e32 v8, 2, v0
	global_load_lds_dwordx4 v[6:7], off
	v_lshlrev_b32_e32 v6, 1, v4
	v_and_b32_e32 v8, 32, v8
	v_lshl_or_b32 v195, s10, 6, v5
	v_lshl_or_b32 v5, v5, 6, v6
	s_lshl_b32 s10, s10, 13
	s_lshl_b32 s9, s9, 5
	v_lshlrev_b32_e32 v7, 6, v0
	s_movk_i32 s11, 0x3c0
	v_bitop3_b32 v5, v5, s10, v8 bitop3:0xde
	s_and_b32 s10, s9, 0x60
	v_and_or_b32 v7, v7, s11, v6
	s_lshl_b32 s9, s10, 7
	v_bitop3_b32 v203, s9, v7, v8 bitop3:0xf6
	s_waitcnt vmcnt(6)
	s_cmpk_lt_u32 s8, 0x100
	v_lshlrev_b32_e32 v210, 2, v2
	v_add_u32_e32 v2, 0, v203
	s_cselect_b64 s[8:9], -1, 0
	v_or_b32_e32 v205, s10, v4
	v_lshlrev_b32_e32 v208, 2, v3
	v_add_u32_e32 v212, 0x10000, v2
	v_add_u32_e32 v213, 0x14000, v2
	v_add_u32_e32 v214, 0, v5
	v_mov_b32_e32 v215, 0x7f7f7f7f
	s_mov_b32 s52, 0xc3e00000
	s_mov_b64 s[10:11], 0x40000
	s_mov_b32 s53, 0x40000
	s_mov_b64 s[12:13], 0x48000
	s_mov_b32 s54, 0x48000
	s_mov_b64 s[14:15], 0x50000
	s_mov_b32 s55, 0x50000
	s_mov_b64 s[16:17], 0x58000
	s_mov_b32 s56, 0x58000
	v_mov_b32_e32 v216, 0x43e00000
	s_barrier
	v_lshl_add_u32 v225, s58, 8, v195
	v_lshlrev_b32_e32 v225, 2, v225
	global_load_dword v240, v225, s[60:61]
	global_load_dword v241, v225, s[60:61] offset:64
	global_load_dword v242, v225, s[60:61] offset:128
	global_load_dword v243, v225, s[60:61] offset:192
	global_load_dword v244, v225, s[60:61] offset:512
	global_load_dword v245, v225, s[60:61] offset:576
	global_load_dword v246, v225, s[60:61] offset:640
	global_load_dword v247, v225, s[60:61] offset:704
	s_branch .LBB0_1958

;     DI void operator()(const f32x4 (&acc)[2][2][4][2], const Unit& u, int wr, int wc, int fr, int fq) const {
;         const int row0 = u.pm * 256 + wr * 64 + fr, col0 = (u.pn & 7) * 256 + wc * 32 + 8 * fq;
;         float gts[2][4];
; #pragma unroll
;         for (int ai = 0; ai < 2; ++ai)
; #pragma unroll
;             for (int m = 0; m < 4; ++m) gts[ai][m] = gatev[row0 + ai * 128 + m * 16];
;         __builtin_amdgcn_sched_barrier(0);
; #pragma unroll
;         for (int ai = 0; ai < 2; ++ai)
; #pragma unroll
;             for (int m = 0; m < 4; ++m) { const int row = row0 + ai * 128 + m * 16; const float gt = gts[ai][m] * ws;
; #pragma unroll
;                 for (int bj = 0; bj < 2; ++bj) { const f32x4 v0 = acc[ai][bj][m][0] * gt, v1 = acc[ai][bj][m][1] * gt;
;                     u32x2 w; w.x = pk4_fp8(v0[0], v0[1], v0[2], v0[3]); w.y = pk4_fp8(v1[0], v1[1], v1[2], v1[3]);
;                     *(u32x2*)((unsigned char*)Y + (size_t)row * DM + col0 + bj * 128) = w; } }
.LBB0_1968:
	s_andn2_b64 vcc, exec, s[20:21]
	s_cbranch_vccnz .Lp17_nopf
	v_lshl_add_u32 v225, s57, 8, v195
	v_lshlrev_b32_e32 v225, 2, v225
	global_load_dword v232, v225, s[60:61]
	global_load_dword v233, v225, s[60:61] offset:64
	global_load_dword v234, v225, s[60:61] offset:128
	global_load_dword v235, v225, s[60:61] offset:192
	global_load_dword v236, v225, s[60:61] offset:512
	global_load_dword v237, v225, s[60:61] offset:576
	global_load_dword v238, v225, s[60:61] offset:640
	global_load_dword v239, v225, s[60:61] offset:704
.Lp17_nopf:
	v_and_b32_e32 v30, 8, v205
	v_lshlrev_b32_e32 v30, 1, v30
	v_add_u32_e32 v30, v30, v195
	v_lshl_add_u32 v30, s58, 8, v30
	v_lshlrev_b32_e32 v224, 11, v30
	s_lshl_b32 s19, s24, 8
	s_and_b32 s19, s19, 0x700
	v_and_b32_e32 v30, 0x70, v205
	v_or_b32_e32 v30, s19, v30
	v_add_u32_e32 v224, v224, v30
	v_add_f32_e32 v26, v240, v240
	v_add_f32_e32 v28, v241, v241
	v_pk_mul_f32 v[2:3], v[190:191], v[26:27] op_sel_hi:[1,0]
	v_pk_mul_f32 v[4:5], v[192:193], v[26:27] op_sel_hi:[1,0]
	v_pk_mul_f32 v[6:7], v[186:187], v[26:27] op_sel_hi:[1,0]
	v_pk_mul_f32 v[8:9], v[188:189], v[26:27] op_sel_hi:[1,0]
	v_pk_mul_f32 v[10:11], v[174:175], v[28:29] op_sel_hi:[1,0]
	v_pk_mul_f32 v[12:13], v[176:177], v[28:29] op_sel_hi:[1,0]
	v_pk_mul_f32 v[14:15], v[170:171], v[28:29] op_sel_hi:[1,0]
	v_pk_mul_f32 v[16:17], v[172:173], v[28:29] op_sel_hi:[1,0]
	v_med3_f32 v2, v2, s52, v216
	v_med3_f32 v3, v3, s52, v216
	v_med3_f32 v4, v4, s52, v216
	v_med3_f32 v5, v5, s52, v216
	v_med3_f32 v6, v6, s52, v216
	v_med3_f32 v7, v7, s52, v216
	v_med3_f32 v8, v8, s52, v216
	v_med3_f32 v9, v9, s52, v216
	v_med3_f32 v10, v10, s52, v216
	v_med3_f32 v11, v11, s52, v216
	v_med3_f32 v12, v12, s52, v216
	v_med3_f32 v13, v13, s52, v216
	v_med3_f32 v14, v14, s52, v216
	v_med3_f32 v15, v15, s52, v216
	v_med3_f32 v16, v16, s52, v216
	v_med3_f32 v17, v17, s52, v216
	v_cvt_pk_fp8_f32 v18, v2, v3
	v_cvt_pk_fp8_f32 v19, v6, v7
	v_cvt_pk_fp8_f32 v20, v10, v11
	v_cvt_pk_fp8_f32 v21, v14, v15
	v_cvt_pk_fp8_f32 v18, v4, v5 op_sel:[0,0,1]
	v_cvt_pk_fp8_f32 v19, v8, v9 op_sel:[0,0,1]
	v_cvt_pk_fp8_f32 v20, v12, v13 op_sel:[0,0,1]
	v_cvt_pk_fp8_f32 v21, v16, v17 op_sel:[0,0,1]
	v_pk_mul_f32 v[2:3], v[182:183], v[26:27] op_sel_hi:[1,0]
	v_pk_mul_f32 v[4:5], v[184:185], v[26:27] op_sel_hi:[1,0]
	v_pk_mul_f32 v[6:7], v[178:179], v[26:27] op_sel_hi:[1,0]
	v_pk_mul_f32 v[8:9], v[180:181], v[26:27] op_sel_hi:[1,0]
	v_pk_mul_f32 v[10:11], v[166:167], v[28:29] op_sel_hi:[1,0]
	v_pk_mul_f32 v[12:13], v[168:169], v[28:29] op_sel_hi:[1,0]
	v_pk_mul_f32 v[14:15], v[162:163], v[28:29] op_sel_hi:[1,0]
	v_pk_mul_f32 v[16:17], v[164:165], v[28:29] op_sel_hi:[1,0]
	v_med3_f32 v2, v2, s52, v216
	v_med3_f32 v3, v3, s52, v216
	v_med3_f32 v4, v4, s52, v216
	v_med3_f32 v5, v5, s52, v216
	v_med3_f32 v6, v6, s52, v216
	v_med3_f32 v7, v7, s52, v216
	v_med3_f32 v8, v8, s52, v216
	v_med3_f32 v9, v9, s52, v216
	v_med3_f32 v10, v10, s52, v216
	v_med3_f32 v11, v11, s52, v216
	v_med3_f32 v12, v12, s52, v216
	v_med3_f32 v13, v13, s52, v216
	v_med3_f32 v14, v14, s52, v216
	v_med3_f32 v15, v15, s52, v216
	v_med3_f32 v16, v16, s52, v216
	v_med3_f32 v17, v17, s52, v216
	v_cvt_pk_fp8_f32 v22, v2, v3
	v_cvt_pk_fp8_f32 v23, v6, v7
	v_cvt_pk_fp8_f32 v24, v10, v11
	v_cvt_pk_fp8_f32 v25, v14, v15
	v_cvt_pk_fp8_f32 v22, v4, v5 op_sel:[0,0,1]
	v_cvt_pk_fp8_f32 v23, v8, v9 op_sel:[0,0,1]
	v_cvt_pk_fp8_f32 v24, v12, v13 op_sel:[0,0,1]
	v_cvt_pk_fp8_f32 v25, v16, v17 op_sel:[0,0,1]
	s_nop 1
	v_permlane16_swap_b32_e32 v18, v20
	v_permlane16_swap_b32_e32 v19, v21
	v_mov_b32_e32 v30, v224
	global_store_dwordx4 v30, v[18:21], s[4:5]
	s_nop 1
	v_permlane16_swap_b32_e32 v22, v24
	v_permlane16_swap_b32_e32 v23, v25
	v_add_u32_e32 v30, 0x80, v224
	global_store_dwordx4 v30, v[22:25], s[4:5]
	v_add_f32_e32 v26, v242, v242
	v_add_f32_e32 v28, v243, v243
	v_pk_mul_f32 v[2:3], v[158:159], v[26:27] op_sel_hi:[1,0]
	v_pk_mul_f32 v[4:5], v[160:161], v[26:27] op_sel_hi:[1,0]
	v_pk_mul_f32 v[6:7], v[154:155], v[26:27] op_sel_hi:[1,0]
	v_pk_mul_f32 v[8:9], v[156:157], v[26:27] op_sel_hi:[1,0]
	v_pk_mul_f32 v[10:11], v[142:143], v[28:29] op_sel_hi:[1,0]
	v_pk_mul_f32 v[12:13], v[144:145], v[28:29] op_sel_hi:[1,0]
	v_pk_mul_f32 v[14:15], v[138:139], v[28:29] op_sel_hi:[1,0]
	v_pk_mul_f32 v[16:17], v[140:141], v[28:29] op_sel_hi:[1,0]
	v_med3_f32 v2, v2, s52, v216
	v_med3_f32 v3, v3, s52, v216
	v_med3_f32 v4, v4, s52, v216
	v_med3_f32 v5, v5, s52, v216
	v_med3_f32 v6, v6, s52, v216
	v_med3_f32 v7, v7, s52, v216
	v_med3_f32 v8, v8, s52, v216
	v_med3_f32 v9, v9, s52, v216
	v_med3_f32 v10, v10, s52, v216
	v_med3_f32 v11, v11, s52, v216
	v_med3_f32 v12, v12, s52, v216
	v_med3_f32 v13, v13, s52, v216
	v_med3_f32 v14, v14, s52, v216
	v_med3_f32 v15, v15, s52, v216
	v_med3_f32 v16, v16, s52, v216
	v_med3_f32 v17, v17, s52, v216
	v_cvt_pk_fp8_f32 v18, v2, v3
	v_cvt_pk_fp8_f32 v19, v6, v7
	v_cvt_pk_fp8_f32 v20, v10, v11
	v_cvt_pk_fp8_f32 v21, v14, v15
	v_cvt_pk_fp8_f32 v18, v4, v5 op_sel:[0,0,1]
	v_cvt_pk_fp8_f32 v19, v8, v9 op_sel:[0,0,1]
	v_cvt_pk_fp8_f32 v20, v12, v13 op_sel:[0,0,1]
	v_cvt_pk_fp8_f32 v21, v16, v17 op_sel:[0,0,1]
	v_pk_mul_f32 v[2:3], v[150:151], v[26:27] op_sel_hi:[1,0]
	v_pk_mul_f32 v[4:5], v[152:153], v[26:27] op_sel_hi:[1,0]
	v_pk_mul_f32 v[6:7], v[146:147], v[26:27] op_sel_hi:[1,0]
	v_pk_mul_f32 v[8:9], v[148:149], v[26:27] op_sel_hi:[1,0]
	v_pk_mul_f32 v[10:11], v[134:135], v[28:29] op_sel_hi:[1,0]
	v_pk_mul_f32 v[12:13], v[136:137], v[28:29] op_sel_hi:[1,0]
	v_pk_mul_f32 v[14:15], v[130:131], v[28:29] op_sel_hi:[1,0]
	v_pk_mul_f32 v[16:17], v[132:133], v[28:29] op_sel_hi:[1,0]
	v_med3_f32 v2, v2, s52, v216
;     DI void operator()(const f32x4 (&acc)[2][2][4][2], const Unit& u, int wr, int wc, int fr, int fq) const {
;     ...
;             for (int m = 0; m < 4; ++m) { const int row = row0 + ai * 128 + m * 16; const float gt = gts[ai][m] * ws;
; #pragma unroll
;                 for (int bj = 0; bj < 2; ++bj) { const f32x4 v0 = acc[ai][bj][m][0] * gt, v1 = acc[ai][bj][m][1] * gt;
;                     u32x2 w; w.x = pk4_fp8(v0[0], v0[1], v0[2], v0[3]); w.y = pk4_fp8(v1[0], v1[1], v1[2], v1[3]);
;                     *(u32x2*)((unsigned char*)Y + (size_t)row * DM + col0 + bj * 128) = w; } }
	v_med3_f32 v3, v3, s52, v216
	v_med3_f32 v4, v4, s52, v216
	v_med3_f32 v5, v5, s52, v216
	v_med3_f32 v6, v6, s52, v216
	v_med3_f32 v7, v7, s52, v216
	v_med3_f32 v8, v8, s52, v216
	v_med3_f32 v9, v9, s52, v216
	v_med3_f32 v10, v10, s52, v216
	v_med3_f32 v11, v11, s52, v216
	v_med3_f32 v12, v12, s52, v216
	v_med3_f32 v13, v13, s52, v216
	v_med3_f32 v14, v14, s52, v216
	v_med3_f32 v15, v15, s52, v216
	v_med3_f32 v16, v16, s52, v216
	v_med3_f32 v17, v17, s52, v216
	v_cvt_pk_fp8_f32 v22, v2, v3
	v_cvt_pk_fp8_f32 v23, v6, v7
	v_cvt_pk_fp8_f32 v24, v10, v11
	v_cvt_pk_fp8_f32 v25, v14, v15
	v_cvt_pk_fp8_f32 v22, v4, v5 op_sel:[0,0,1]
	v_cvt_pk_fp8_f32 v23, v8, v9 op_sel:[0,0,1]
	v_cvt_pk_fp8_f32 v24, v12, v13 op_sel:[0,0,1]
	v_cvt_pk_fp8_f32 v25, v16, v17 op_sel:[0,0,1]
	s_nop 1
	v_permlane16_swap_b32_e32 v18, v20
	v_permlane16_swap_b32_e32 v19, v21
	v_add_u32_e32 v30, 0x10000, v224
	global_store_dwordx4 v30, v[18:21], s[4:5]
	s_nop 1
	v_permlane16_swap_b32_e32 v22, v24
	v_permlane16_swap_b32_e32 v23, v25
	v_add_u32_e32 v30, 0x10080, v224
	global_store_dwordx4 v30, v[22:25], s[4:5]
	v_add_f32_e32 v26, v244, v244
	v_add_f32_e32 v28, v245, v245
	v_pk_mul_f32 v[2:3], v[126:127], v[26:27] op_sel_hi:[1,0]
	v_pk_mul_f32 v[4:5], v[128:129], v[26:27] op_sel_hi:[1,0]
	v_pk_mul_f32 v[6:7], v[122:123], v[26:27] op_sel_hi:[1,0]
	v_pk_mul_f32 v[8:9], v[124:125], v[26:27] op_sel_hi:[1,0]
	v_pk_mul_f32 v[10:11], v[110:111], v[28:29] op_sel_hi:[1,0]
	v_pk_mul_f32 v[12:13], v[112:113], v[28:29] op_sel_hi:[1,0]
	v_pk_mul_f32 v[14:15], v[106:107], v[28:29] op_sel_hi:[1,0]
	v_pk_mul_f32 v[16:17], v[108:109], v[28:29] op_sel_hi:[1,0]
	v_med3_f32 v2, v2, s52, v216
	v_med3_f32 v3, v3, s52, v216
	v_med3_f32 v4, v4, s52, v216
	v_med3_f32 v5, v5, s52, v216
	v_med3_f32 v6, v6, s52, v216
	v_med3_f32 v7, v7, s52, v216
	v_med3_f32 v8, v8, s52, v216
	v_med3_f32 v9, v9, s52, v216
	v_med3_f32 v10, v10, s52, v216
	v_med3_f32 v11, v11, s52, v216
	v_med3_f32 v12, v12, s52, v216
	v_med3_f32 v13, v13, s52, v216
	v_med3_f32 v14, v14, s52, v216
	v_med3_f32 v15, v15, s52, v216
	v_med3_f32 v16, v16, s52, v216
	v_med3_f32 v17, v17, s52, v216
	v_cvt_pk_fp8_f32 v18, v2, v3
	v_cvt_pk_fp8_f32 v19, v6, v7
	v_cvt_pk_fp8_f32 v20, v10, v11
	v_cvt_pk_fp8_f32 v21, v14, v15
	v_cvt_pk_fp8_f32 v18, v4, v5 op_sel:[0,0,1]
	v_cvt_pk_fp8_f32 v19, v8, v9 op_sel:[0,0,1]
	v_cvt_pk_fp8_f32 v20, v12, v13 op_sel:[0,0,1]
	v_cvt_pk_fp8_f32 v21, v16, v17 op_sel:[0,0,1]
	v_pk_mul_f32 v[2:3], v[118:119], v[26:27] op_sel_hi:[1,0]
	v_pk_mul_f32 v[4:5], v[120:121], v[26:27] op_sel_hi:[1,0]
	v_pk_mul_f32 v[6:7], v[114:115], v[26:27] op_sel_hi:[1,0]
	v_pk_mul_f32 v[8:9], v[116:117], v[26:27] op_sel_hi:[1,0]
	v_pk_mul_f32 v[10:11], v[94:95], v[28:29] op_sel_hi:[1,0]
	v_pk_mul_f32 v[12:13], v[96:97], v[28:29] op_sel_hi:[1,0]
	v_pk_mul_f32 v[14:15], v[82:83], v[28:29] op_sel_hi:[1,0]
	v_pk_mul_f32 v[16:17], v[84:85], v[28:29] op_sel_hi:[1,0]
	v_med3_f32 v2, v2, s52, v216
	v_med3_f32 v3, v3, s52, v216
	v_med3_f32 v4, v4, s52, v216
	v_med3_f32 v5, v5, s52, v216
	v_med3_f32 v6, v6, s52, v216
	v_med3_f32 v7, v7, s52, v216
	v_med3_f32 v8, v8, s52, v216
	v_med3_f32 v9, v9, s52, v216
	v_med3_f32 v10, v10, s52, v216
	v_med3_f32 v11, v11, s52, v216
	v_med3_f32 v12, v12, s52, v216
	v_med3_f32 v13, v13, s52, v216
	v_med3_f32 v14, v14, s52, v216
	v_med3_f32 v15, v15, s52, v216
	v_med3_f32 v16, v16, s52, v216
	v_med3_f32 v17, v17, s52, v216
	v_cvt_pk_fp8_f32 v22, v2, v3
	v_cvt_pk_fp8_f32 v23, v6, v7
	v_cvt_pk_fp8_f32 v24, v10, v11
	v_cvt_pk_fp8_f32 v25, v14, v15
	v_cvt_pk_fp8_f32 v22, v4, v5 op_sel:[0,0,1]
	v_cvt_pk_fp8_f32 v23, v8, v9 op_sel:[0,0,1]
	v_cvt_pk_fp8_f32 v24, v12, v13 op_sel:[0,0,1]
	v_cvt_pk_fp8_f32 v25, v16, v17 op_sel:[0,0,1]
	s_nop 1
	v_permlane16_swap_b32_e32 v18, v20
	v_permlane16_swap_b32_e32 v19, v21
	v_add_u32_e32 v30, 0x40000, v224
	global_store_dwordx4 v30, v[18:21], s[4:5]
	s_nop 1
	v_permlane16_swap_b32_e32 v22, v24
	v_permlane16_swap_b32_e32 v23, v25
	v_add_u32_e32 v30, 0x40080, v224
	global_store_dwordx4 v30, v[22:25], s[4:5]
	v_add_f32_e32 v26, v246, v246
	v_add_f32_e32 v28, v247, v247
	v_pk_mul_f32 v[2:3], v[90:91], v[26:27] op_sel_hi:[1,0]
	v_pk_mul_f32 v[4:5], v[92:93], v[26:27] op_sel_hi:[1,0]
	v_pk_mul_f32 v[6:7], v[86:87], v[26:27] op_sel_hi:[1,0]
	v_pk_mul_f32 v[8:9], v[88:89], v[26:27] op_sel_hi:[1,0]
	v_pk_mul_f32 v[10:11], v[70:71], v[28:29] op_sel_hi:[1,0]
	v_pk_mul_f32 v[12:13], v[72:73], v[28:29] op_sel_hi:[1,0]
	v_pk_mul_f32 v[14:15], v[66:67], v[28:29] op_sel_hi:[1,0]
	v_pk_mul_f32 v[16:17], v[68:69], v[28:29] op_sel_hi:[1,0]
	v_med3_f32 v2, v2, s52, v216
	v_med3_f32 v3, v3, s52, v216
	v_med3_f32 v4, v4, s52, v216
	v_med3_f32 v5, v5, s52, v216
	v_med3_f32 v6, v6, s52, v216
	v_med3_f32 v7, v7, s52, v216
	v_med3_f32 v8, v8, s52, v216
	v_med3_f32 v9, v9, s52, v216
	v_med3_f32 v10, v10, s52, v216
	v_med3_f32 v11, v11, s52, v216
	v_med3_f32 v12, v12, s52, v216
	v_med3_f32 v13, v13, s52, v216
	v_med3_f32 v14, v14, s52, v216
	v_med3_f32 v15, v15, s52, v216
	v_med3_f32 v16, v16, s52, v216
	v_med3_f32 v17, v17, s52, v216
	v_cvt_pk_fp8_f32 v18, v2, v3
	v_cvt_pk_fp8_f32 v19, v6, v7
	v_cvt_pk_fp8_f32 v20, v10, v11
	v_cvt_pk_fp8_f32 v21, v14, v15
	v_cvt_pk_fp8_f32 v18, v4, v5 op_sel:[0,0,1]
	v_cvt_pk_fp8_f32 v19, v8, v9 op_sel:[0,0,1]
	v_cvt_pk_fp8_f32 v20, v12, v13 op_sel:[0,0,1]
	v_cvt_pk_fp8_f32 v21, v16, v17 op_sel:[0,0,1]
	v_pk_mul_f32 v[2:3], v[98:99], v[26:27] op_sel_hi:[1,0]
	v_pk_mul_f32 v[4:5], v[100:101], v[26:27] op_sel_hi:[1,0]
	v_pk_mul_f32 v[6:7], v[102:103], v[26:27] op_sel_hi:[1,0]
	v_pk_mul_f32 v[8:9], v[104:105], v[26:27] op_sel_hi:[1,0]
	v_pk_mul_f32 v[10:11], v[74:75], v[28:29] op_sel_hi:[1,0]
	v_pk_mul_f32 v[12:13], v[76:77], v[28:29] op_sel_hi:[1,0]
	v_pk_mul_f32 v[14:15], v[78:79], v[28:29] op_sel_hi:[1,0]
	v_pk_mul_f32 v[16:17], v[80:81], v[28:29] op_sel_hi:[1,0]
	v_med3_f32 v2, v2, s52, v216
	v_med3_f32 v3, v3, s52, v216
	v_med3_f32 v4, v4, s52, v216
	v_med3_f32 v5, v5, s52, v216
	v_med3_f32 v6, v6, s52, v216
	v_med3_f32 v7, v7, s52, v216
	v_med3_f32 v8, v8, s52, v216
	v_med3_f32 v9, v9, s52, v216
	v_med3_f32 v10, v10, s52, v216
	v_med3_f32 v11, v11, s52, v216
	v_med3_f32 v12, v12, s52, v216
	v_med3_f32 v13, v13, s52, v216
	v_med3_f32 v14, v14, s52, v216
	v_med3_f32 v15, v15, s52, v216
	v_med3_f32 v16, v16, s52, v216
	v_med3_f32 v17, v17, s52, v216
	v_cvt_pk_fp8_f32 v22, v2, v3
	v_cvt_pk_fp8_f32 v23, v6, v7
	v_cvt_pk_fp8_f32 v24, v10, v11
	v_cvt_pk_fp8_f32 v25, v14, v15
	v_cvt_pk_fp8_f32 v22, v4, v5 op_sel:[0,0,1]
	v_cvt_pk_fp8_f32 v23, v8, v9 op_sel:[0,0,1]
	v_cvt_pk_fp8_f32 v24, v12, v13 op_sel:[0,0,1]
	v_cvt_pk_fp8_f32 v25, v16, v17 op_sel:[0,0,1]
	s_nop 1
	v_permlane16_swap_b32_e32 v18, v20
	v_permlane16_swap_b32_e32 v19, v21
	v_add_u32_e32 v30, 0x50000, v224
	global_store_dwordx4 v30, v[18:21], s[4:5]
	s_nop 1
	v_permlane16_swap_b32_e32 v22, v24
	v_permlane16_swap_b32_e32 v23, v25
	v_add_u32_e32 v30, 0x50080, v224
	global_store_dwordx4 v30, v[22:25], s[4:5]
	s_andn2_b64 vcc, exec, s[20:21]
	s_cbranch_vccnz .Lp17_nocp
; #define PG8_BAR __builtin_amdgcn_s_barrier()
; template <class Epi, class Sched, bool ALIGN_EPI = false, bool SP2 = false, bool GATHER = false, bool F8 = false>
; __device__ __forceinline__ void gemm_phase(PG8_LAS unsigned char* lds, const Gemm g, const Sched& S, const Epi& E) {
;     ...
;         if constexpr (!Epi::AFTER_DRAIN) { E(acc, cur, wr, wc, fr, fq); S.done(cur); }
;         if (!has_next) break;
; #pragma unroll
;         for (int a = 0; a < 2; ++a)
; #pragma unroll
;             for (int b = 0; b < 2; ++b)
; #pragma unroll
;                 for (int m = 0; m < 4; ++m)
; #pragma unroll
;                     for (int n = 0; n < 2; ++n) acc[a][b][m][n] = (f32x4){0.f, 0.f, 0.f, 0.f};
;         cur = nxt; cA = nA; cB = nB; ++ui;
;         if constexpr (ALIGN_EPI) { if (wr == 1) PG8_BAR; }
	s_waitcnt vmcnt(8)
	v_mov_b32_e32 v240, v232
	v_mov_b32_e32 v241, v233
	v_mov_b32_e32 v242, v234
	v_mov_b32_e32 v243, v235
	v_mov_b32_e32 v244, v236
	v_mov_b32_e32 v245, v237
	v_mov_b32_e32 v246, v238
	v_mov_b32_e32 v247, v239
.Lp17_nocp:
	s_andn2_b64 vcc, exec, s[20:21]
	s_mov_b64 s[20:21], -1
	s_cbranch_vccnz .LBB0_1957
	s_andn2_b64 vcc, exec, s[6:7]
	s_cbranch_vccnz .LBB0_1956
	s_barrier
	s_branch .LBB0_1956
